# speedup vs baseline: 1.0230x; 1.0061x over previous
.LBB0_19:
	s_and_b64 vcc, exec, s[2:3]
	s_cbranch_vccz .LBB0_114
	s_setprio 3
	s_load_dwordx2 s[4:5], s[0:1], 0x40
	s_load_dwordx2 s[2:3], s[0:1], 0x0
	v_lshl_or_b32 v2, s26, 10, v0
	v_add_u32_e32 v7, 0xfff9e400, v2
	v_and_b32_e32 v2, 31, v0
	v_lshlrev_b32_e32 v4, 5, v2
	v_mov_b32_e32 v5, 0
	s_waitcnt lgkmcnt(0)
	v_lshl_add_u64 v[2:3], s[2:3], 0, v[4:5]
	v_mul_u32_u24_e32 v6, 0xc350, v1
	v_lshlrev_b32_e32 v1, 4, v0
	s_mov_b32 s2, 0x186a00
	s_mov_b32 s7, 0x20000
	s_mov_b32 s6, 0x186a000
	s_and_b32 s5, s5, 0xffff
	v_and_b32_e32 v1, 0x70, v1
	v_cmp_gt_u32_e32 vcc, s2, v7
	s_and_saveexec_b64 s[2:3], vcc
	s_cbranch_execz .LBB0_22
	v_lshrrev_b32_e32 v16, 5, v7
	v_lshlrev_b32_e32 v4, 10, v16
	v_lshl_add_u64 v[4:5], v[2:3], 0, v[4:5]
	global_load_dwordx4 v[8:11], v[4:5], off offset:16 nt
	global_load_dwordx4 v[12:15], v[4:5], off nt
	v_add_u32_e32 v4, v16, v6
	v_lshl_or_b32 v4, v4, 7, v1
	s_waitcnt vmcnt(1)
	v_cvt_pk_f16_f32 v11, v10, v11
	v_cvt_pk_f16_f32 v10, v8, v9
	s_waitcnt vmcnt(0)
	v_cvt_pk_f16_f32 v9, v14, v15
	v_cvt_pk_f16_f32 v8, v12, v13
	buffer_store_dwordx4 v[8:11], v4, s[4:7], 0 offen sc1
